# conv_w tile->block remap so each XCD produces the xs rows / W^T tiles its own qkv/wo blocks read
# speedup vs baseline: 1.0434x; 1.0434x over previous
_Z13conv_w_kernelPKfS0_S0_S0_PDF16_S1_S0_S1_:
	s_cmp_gt_u32 s4, 1
	s_cbranch_scc1 .Lcw_w
	s_and_b32 s5, s2, 1
	s_lshr_b32 s2, s2, 1
	s_lshl_b32 s4, s4, 4
	s_or_b32 s2, s2, s4
	s_mov_b32 s4, s5
	s_branch .Lcw_done
.Lcw_w:
	s_and_b32 s5, s2, 7
	s_lshr_b32 s6, s2, 3
	s_sub_i32 s7, s4, 2
	s_lshl_b32 s7, s7, 2
	s_add_i32 s7, s7, s6
	s_cmp_lt_u32 s7, 8
	s_cbranch_scc0 .Lcw_hi
	s_and_b32 s2, s5, 3
	s_lshl_b32 s2, s2, 3
	s_add_i32 s2, s2, s7
	s_lshr_b32 s4, s5, 2
	s_add_i32 s4, s4, 2
	s_branch .Lcw_done
.Lcw_hi:
	s_and_b32 s6, s7, 3
	s_lshl_b32 s2, s5, 2
	s_add_i32 s2, s2, s6
	s_lshr_b32 s4, s7, 2
	s_add_i32 s4, s4, 2
.Lcw_done:
	s_cmp_gt_u32 s4, 1
	s_mov_b64 s[6:7], -1
	s_cbranch_scc1 .LBB1_3
	s_and_b64 vcc, exec, s[6:7]
	s_cbranch_vccnz .LBB1_12
